# attention hot loop: K/V tile LDS-DMA addresses formed as scalar base (SALU adds) plus a 32-bit per-lane offset instead of 64-bit per-lane VALU adds (16 fewer VALU ops per two tiles); plus previous cha
# baseline (speedup 1.0000x reference)
; #define LAS __attribute__((address_space(3)))
; #define AT_DMA_K(j, so) do { const char* _p = pb + (size_t)__builtin_amdgcn_readfirstlane(AT_ROW(j)) * (INW * 2); \
;         __builtin_amdgcn_global_load_lds((const unsigned*)(_p + dK), (LAS unsigned*)(lds + (so) + SHM_V + widu * 1024), 16, 0, 0); } while (0)
; __device__ __forceinline__ void expSM(f32x16& p) {
; #pragma unroll
;     for (int r = 0; r < 16; ++r) p[r] = __builtin_amdgcn_exp2f(p[r]);
; }
; __device__ __forceinline__ void finishFast(f32x16& p0, f32x16& p1, bool& ovf, float& l_reg, bf16x8& pa0, bf16x8& pa1, bf16x8& pa2, bf16x8& pa3) {
;     expSM(p1);
;     typedef float f32x2_t __attribute__((ext_vector_type(2)));
;     f32x2_t sa = {p0[0], p0[1]}, sb = {p0[8], p0[9]}, sc = {p1[0], p1[1]}, sd = {p1[8], p1[9]};
; #pragma unroll
;     for (int r = 2; r < 8; r += 2) { sa += f32x2_t{p0[r], p0[r + 1]}; sb += f32x2_t{p0[8 + r], p0[9 + r]}; sc += f32x2_t{p1[r], p1[r + 1]}; sd += f32x2_t{p1[8 + r], p1[9 + r]}; }
;     const f32x2_t ps2 = (sa + sb) + (sc + sd);
;     float ps = ps2.x + ps2.y;
;     { auto rr = __builtin_amdgcn_permlane32_swap(__float_as_uint(ps), __float_as_uint(ps), false, false);
;       ps = __uint_as_float(rr[0]) + __uint_as_float(rr[1]); }
;     l_reg += ps;
; template <bool ROBUST>
; __device__ __forceinline__ bool attn_pass(const bf16_t* __restrict__ proj, LAS char* lds, int qrow0, int ctxrow0, int latrow0, int NT, int h, int comp, f32x16 (&o)[4]) {
;     ...
;     AT_DMA_K(0, 0); AT_DMA_V(0, 0); AT_DMA_K(1, SLOT); AT_DMA_V(1, SLOT); AT_DMA_K(2, 2 * SLOT);
;     asm volatile("s_waitcnt vmcnt(4)" ::: "memory"); __syncthreads();
;     if (tid == 0) *(LAS int*)(lds + OFF_FLAG) = 0;
;     qkt(pA0, pA1, lds + SHM_V, qr, r32, hi, 0.f); partialSM<true>(pA0, pA1, m_reg, alA);
;     asm volatile("s_waitcnt vmcnt(1)" ::: "memory"); __syncthreads();
;     AT_DMA_K(3, 0);
;     AT_HALF(false, pB0, pB1, pA0, pA1, 1);
;     for (int j = 2; j + 1 < NT; j += 2) {
;         AT_HALF(true, pA0, pA1, pB0, pB1, j);
;         AT_HALF(true, pB0, pB1, pA0, pA1, j + 1);
.LBB0_384:
	v_exp_f32_e32 v80, v130
	v_exp_f32_e32 v81, v131
	v_exp_f32_e32 v178, v132
	v_exp_f32_e32 v179, v133
	v_exp_f32_e32 v180, v134
	v_exp_f32_e32 v181, v135
	v_exp_f32_e32 v182, v136
	v_exp_f32_e32 v183, v137
	v_exp_f32_e32 v184, v138
	v_exp_f32_e32 v185, v139
	v_exp_f32_e32 v186, v140
	v_exp_f32_e32 v187, v141
	v_exp_f32_e32 v188, v142
	v_exp_f32_e32 v189, v143
	v_exp_f32_e32 v190, v144
	v_exp_f32_e32 v191, v145
	v_add_f32_e32 v130, v174, v175
	v_add_f32_e32 v130, 0, v130
	v_add_f32_e32 v131, v176, v177
	v_add_f32_e32 v130, v130, v131
	v_add_f32_e32 v67, v192, v67
	s_and_b64 vcc, exec, s[44:45]
	v_add_f32_e32 v204, v130, v67
	s_cbranch_vccnz .LBB0_420
	v_mov_b32_e32 v174, v146
	s_mov_b32 s2, 4
	s_mov_b32 s0, 0xc000
	s_movk_i32 s1, 0x6000
	s_mov_b32 s8, 0
	s_mov_b32 s44, s63

; template <bool ROBUST>
; __device__ __forceinline__ bool attn_pass(const bf16_t* __restrict__ proj, LAS char* lds, int qrow0, int ctxrow0, int latrow0, int NT, int h, int comp, f32x16 (&o)[4]) {
;     ...
;     s16x4 dl0, dh0, dl1, dh1, dl2, dh2, dl3, dh3;
;     int sV = 0, sK = SLOT, sN = 2 * SLOT;
;     ...
;     const bool grpB = widu >= 4;
.LBB0_391:
	s_add_i32 s8, s44, 0xffffff40
	s_ashr_i32 s9, s8, 31
	s_lshl_b64 s[8:9], s[8:9], 13
	s_add_u32 s8, s8, s48
	s_addc_u32 s9, s9, s49
	s_add_u32 s100, s8, s38
	s_addc_u32 s101, s9, s39
	s_add_u32 s8, s8, s4
	s_addc_u32 s9, s9, s5
	s_add_i32 m0, s79, s0
	s_barrier
	global_load_lds_dwordx4 v172, s[100:101]
	s_add_i32 s100, s79, s0
	s_add_i32 m0, s100, 0x400
	s_cmp_ge_u32 s2, s74
	global_load_lds_dwordx4 v172, s[8:9]
	s_cbranch_scc1 .LBB0_393
	s_sub_i32 s8, s44, 64
	s_ashr_i32 s9, s8, 31
	s_lshl_b64 s[8:9], s[8:9], 13
	s_add_u32 s8, s8, s48
	s_addc_u32 s9, s9, s49
	s_add_i32 s100, s78, s7
	s_add_i32 m0, s100, 0x4000
	s_nop 0
	global_load_lds_dwordx4 v174, s[8:9]

; template <bool ROBUST>
; __device__ __forceinline__ bool attn_pass(const bf16_t* __restrict__ proj, LAS char* lds, int qrow0, int ctxrow0, int latrow0, int NT, int h, int comp, f32x16 (&o)[4]) {
;     ...
;     s16x4 dl0, dh0, dl1, dh1, dl2, dh2, dl3, dh3;
;     int sV = 0, sK = SLOT, sN = 2 * SLOT;
;     ...
;     const bool grpB = widu >= 4;
.LBB0_405:
	s_cmp_ge_u32 s2, s65
	s_barrier
	s_cbranch_scc1 .LBB0_407
	s_add_i32 s8, s44, 0xffffff80
	s_ashr_i32 s9, s8, 31
	s_lshl_b64 s[8:9], s[8:9], 13
	s_add_u32 s8, s8, s48
	s_addc_u32 s9, s9, s49
	s_add_u32 s100, s8, s38
	s_addc_u32 s101, s9, s39
	s_add_u32 s8, s8, s4
	s_addc_u32 s9, s9, s5
	s_add_i32 m0, s79, s1
	s_nop 0
	global_load_lds_dwordx4 v172, s[100:101]
	s_add_i32 s100, s79, s1
	s_add_i32 m0, s100, 0x400
	s_nop 0
	global_load_lds_dwordx4 v172, s[8:9]
.LBB0_407:
	s_cmp_ge_u32 s2, s75
	s_cbranch_scc1 .LBB0_409
	s_ashr_i32 s45, s44, 31
	s_lshl_b64 s[8:9], s[44:45], 13
	s_add_u32 s8, s8, s48
	s_addc_u32 s9, s9, s49
	s_add_i32 s100, s78, s0
	s_add_i32 m0, s100, 0x4000
	s_nop 0
	global_load_lds_dwordx4 v174, s[8:9]
